# expert key-table conversion hosted in HGRN2 pass-A chunk loop (experiment on top of v5)
# baseline (speedup 1.0000x reference)
.LBB0_1367:
	s_mov_b64 s[6:7], s[0:1]
	s_barrier
	s_mov_b64 s[6:7], s[0:1]
	s_mov_b64 s[8:9], s[0:1]
	s_mov_b64 s[10:11], s[0:1]
	s_mov_b64 s[12:13], s[0:1]
	v_mov_b32_e32 v2, v0
	s_cmpk_gt_i32 s2, 0xef
	v_readfirstlane_b32 s24, v2
	s_cbranch_scc1 .LBB0_1386
	s_load_dwordx2 s[14:15], s[6:7], 0x90
	s_load_dwordx2 s[16:17], s[8:9], 0x90
	s_load_dwordx2 s[18:19], s[10:11], 0x90
	s_load_dwordx2 s[34:35], s[12:13], 0x90
	v_ashrrev_i32_e32 v6, 3, v2
	s_waitcnt lgkmcnt(0)
	s_add_u32 s28, s14, 0x28400000
	s_addc_u32 s29, s15, 0
	s_add_u32 s30, s16, 0x2c400000
	v_and_b32_e32 v6, -8, v6
	s_addc_u32 s31, s17, 0
	v_lshlrev_b32_e32 v4, 1, v2
	v_ashrrev_i32_e32 v7, 31, v6
	s_add_u32 s3, s18, 0x30400000
	v_and_b32_e32 v5, 0x7e, v4
	v_lshlrev_b64 v[50:51], 7, v[6:7]
	s_movk_i32 s25, 0x90
	v_and_b32_e32 v3, 63, v2
	s_addc_u32 s42, s19, 0
	v_or_b32_e32 v50, v50, v5
	s_add_i32 s6, 0, 0x1c400
	v_lshlrev_b32_e32 v7, 2, v5
	v_mad_u32_u24 v8, v5, s25, 0
	v_and_b32_e32 v5, 15, v2
	v_ashrrev_i32_e32 v6, 6, v2
	v_add_u32_e32 v64, s6, v7
	s_ashr_i32 s36, s24, 2
	v_mad_u32_u24 v68, v5, s25, 0
	v_or_b32_e32 v5, 48, v3
	v_lshl_add_u32 v65, v6, 9, v64
	v_cmp_lt_i32_e64 s[8:9], 7, v6
	v_cmp_lt_i32_e64 s[10:11], 6, v6
	v_cmp_lt_i32_e64 s[12:13], 5, v6
	v_cmp_lt_i32_e64 s[14:15], 4, v6
	v_cmp_lt_i32_e64 s[16:17], 3, v6
	v_cmp_lt_i32_e64 s[18:19], 2, v6
	v_cmp_lt_i32_e64 s[20:21], 1, v6
	v_cmp_lt_i32_e64 s[22:23], 0, v6
	v_lshlrev_b32_e32 v9, 4, v6
	s_and_b32 s37, s36, -16
	v_bfi_b32 v6, -16, s36, v2
	v_mad_u32_u24 v12, v5, s25, 0
	v_or_b32_e32 v5, 0x70, v3
	s_andn2_b32 s24, s24, 63
	s_add_i32 s38, 0, 0x1d400
	s_lshl_b32 s37, s37, 2
	v_mul_lo_u32 v6, v6, s25
	v_mad_u32_u24 v13, v5, s25, 0
	s_ashr_i32 s25, s24, 31
	v_ashrrev_i32_e32 v5, 31, v4
	v_cmp_gt_u32_e64 s[6:7], 64, v2
	s_add_i32 s37, s38, s37
	v_and_b32_e32 v66, 48, v2
	v_add_u32_e32 v10, 0, v6
	v_add_u32_e32 v11, 0xd000, v68
	v_add_u32_e32 v69, s38, v7
	v_or_b32_e32 v6, s24, v3
	v_mov_b32_e32 v7, s25
	v_cmp_gt_i32_e64 s[24:25], 64, v2
	v_lshl_add_u64 v[2:3], v[4:5], 2, s[34:35]
	s_mov_b64 s[34:35], 0x32400000
	v_add_u32_e32 v67, s37, v66
	v_lshl_add_u64 v[52:53], v[2:3], 0, s[34:35]
	v_lshlrev_b64 v[54:55], 4, v[6:7]
	s_movk_i32 s43, 0x7fff
	s_mov_b32 s52, 0xffff0000
	s_mov_b32 s53, 0xffff
	v_add_u32_e32 v70, v8, v9
	v_add_u32_e32 v71, v10, v66
	v_add_u32_e32 v72, v12, v66
	v_add_u32_e32 v73, v11, v66
	v_add_u32_e32 v74, v13, v66
	v_mov_b32_e32 v75, 1
	s_mov_b32 s54, s2
	s_load_dwordx2 s[94:95], s[0:1], 0x78
	s_load_dwordx2 s[96:97], s[0:1], 0x90
	v_mbcnt_hi_u32_b32 v246, -1, v1
	v_mov_b32_e32 v227, 0
	v_ashrrev_i32_e32 v232, 6, v0
	v_mov_b32_e32 v233, 0x260
	v_mov_b32_e32 v234, 0x41700000
	v_lshlrev_b32_e32 v226, 4, v246
	v_lshlrev_b32_e32 v228, 2, v246
	v_and_b32_e32 v247, 64, v246
	v_add_u32_e32 v247, 64, v247
	v_xor_b32_e32 v248, 32, v246
	v_xor_b32_e32 v249, 16, v246
	v_xor_b32_e32 v250, 1, v246
	v_xor_b32_e32 v251, 2, v246
	v_xor_b32_e32 v252, 4, v246
	v_xor_b32_e32 v253, 8, v246
	s_waitcnt lgkmcnt(0)
	s_add_u32 s98, s96, 0xe300000
	s_addc_u32 s99, s97, 0
	s_add_u32 s96, s96, 0xa300000
	s_addc_u32 s97, s97, 0
	s_branch .LBB0_1370

.LBB0_1378:
	s_cmp_lt_u32 s55, 11
	s_cselect_b32 s35, 8, 7
	s_and_b64 s[38:39], s[38:39], exec
	s_cselect_b32 s38, 9, s35
	s_ashr_i32 s35, s34, 31
	s_ashr_i32 s37, s36, 31
	s_lshl_b64 s[56:57], s[34:35], 20
	s_lshl_b64 s[40:41], s[36:37], 13
	v_lshl_add_u64 v[58:59], v[50:51], 0, s[56:57]
	v_lshl_add_u64 v[2:3], s[40:41], 0, v[58:59]
	v_lshlrev_b64 v[2:3], 1, v[2:3]
	v_lshl_add_u64 v[4:5], s[30:31], 0, v[2:3]
	v_lshl_add_u64 v[2:3], s[28:29], 0, v[2:3]
	s_mov_b32 s60, 0
	s_min_u32 s60, s60, 6
	s_mul_i32 s61, s54, 7
	s_add_i32 s60, s60, s61
	v_mov_b32_e32 v162, s60
	s_mov_b64 s[62:63], s[94:95]
	s_mov_b64 s[64:65], s[94:95]
	s_movk_i32 s72, 0x1000
	s_movk_i32 s73, 0x3fff
	s_movk_i32 s74, 0x2000
	s_movk_i32 s75, 0x3000
	v_lshl_add_u32 v162, v162, 3, v232
	v_add_u32_e32 v163, 0xffffc000, v162
	v_cmp_lt_i32_e64 s[86:87], s73, v162
	v_mov_b32_e32 v164, s64
	s_nop 0
	v_cndmask_b32_e64 v230, v162, v163, s[86:87]
	v_mov_b32_e32 v162, s63
	v_mov_b32_e32 v163, s65
	v_cndmask_b32_e64 v163, v162, v163, s[86:87]
	v_mov_b32_e32 v162, s62
	v_ashrrev_i32_e32 v231, 31, v230
	v_cndmask_b32_e64 v162, v162, v164, s[86:87]
	v_lshlrev_b64 v[164:165], 14, v[230:231]
	v_lshl_add_u64 v[162:163], v[162:163], 0, v[164:165]
	v_lshl_add_u64 v[162:163], v[162:163], 0, v[226:227]
	v_add_co_u32_e32 v194, vcc, s74, v162
	global_load_dwordx4 v[206:209], v[162:163], off
	global_load_dwordx4 v[190:193], v[162:163], off offset:1024
	global_load_dwordx4 v[186:189], v[162:163], off offset:2048
	global_load_dwordx4 v[178:181], v[162:163], off offset:3072
	v_addc_co_u32_e32 v195, vcc, 0, v163, vcc
	global_load_dwordx4 v[182:185], v[194:195], off offset:-4096
	v_add_co_u32_e32 v164, vcc, s72, v162
	s_nop 0
	s_nop 0
	v_addc_co_u32_e32 v165, vcc, 0, v163, vcc
	global_load_dwordx4 v[170:173], v[164:165], off offset:1024
	v_add_co_u32_e32 v196, vcc, s75, v162
	s_nop 0
	s_nop 0
	v_addc_co_u32_e32 v197, vcc, 0, v163, vcc
	global_load_dwordx4 v[222:225], v[164:165], off offset:2048
	global_load_dwordx4 v[210:213], v[164:165], off offset:3072
	global_load_dwordx4 v[198:201], v[194:195], off
	global_load_dwordx4 v[174:177], v[194:195], off offset:1024
	global_load_dwordx4 v[166:169], v[194:195], off offset:2048
	s_nop 0
	global_load_dwordx4 v[162:165], v[196:197], off offset:3072
	global_load_dwordx4 v[136:139], v[194:195], off offset:3072
	global_load_dwordx4 v[140:143], v[196:197], off
	global_load_dwordx4 v[144:147], v[196:197], off offset:1024
	global_load_dwordx4 v[148:151], v[196:197], off offset:2048
	global_load_dword v76, v[4:5], off
	global_load_dword v77, v[4:5], off offset:256
	global_load_dword v78, v[4:5], off offset:512
	global_load_dword v79, v[4:5], off offset:768
	global_load_dword v80, v[4:5], off offset:1024
	global_load_dword v81, v[4:5], off offset:1280
	global_load_dword v82, v[4:5], off offset:1536
	global_load_dword v83, v[4:5], off offset:1792
	global_load_dword v84, v[2:3], off
	global_load_dword v85, v[2:3], off offset:256
	global_load_dword v86, v[2:3], off offset:512
	global_load_dword v87, v[2:3], off offset:768
	global_load_dword v88, v[2:3], off offset:1024
	global_load_dword v89, v[2:3], off offset:1280
	global_load_dword v90, v[2:3], off offset:1536
	global_load_dword v91, v[2:3], off offset:1792
	v_mov_b32_e32 v56, 0
	s_add_i32 s35, s36, 1
	s_mov_b32 s39, 0
	v_mov_b32_e32 v57, v56
	v_mov_b32_e32 v22, v56
	v_mov_b32_e32 v23, v56
	v_mov_b32_e32 v24, v56
	v_mov_b32_e32 v25, v56
	v_mov_b32_e32 v18, v56
	v_mov_b32_e32 v19, v56
	v_mov_b32_e32 v20, v56
	v_mov_b32_e32 v21, v56
	v_mov_b32_e32 v26, v56
	v_mov_b32_e32 v27, v56
	v_mov_b32_e32 v28, v56
	v_mov_b32_e32 v29, v56
	v_mov_b32_e32 v30, v56
	v_mov_b32_e32 v31, v56
	v_mov_b32_e32 v32, v56
	v_mov_b32_e32 v33, v56
	v_mov_b32_e32 v10, v56
	v_mov_b32_e32 v11, v56
	v_mov_b32_e32 v12, v56
	v_mov_b32_e32 v13, v56
	v_mov_b32_e32 v6, v56
	v_mov_b32_e32 v7, v56
	v_mov_b32_e32 v8, v56
	v_mov_b32_e32 v9, v56
	v_mov_b32_e32 v14, v56
	v_mov_b32_e32 v15, v56
	v_mov_b32_e32 v16, v56
	v_mov_b32_e32 v17, v56
	v_mov_b32_e32 v2, v56
	v_mov_b32_e32 v3, v56
	v_mov_b32_e32 v4, v56
	v_mov_b32_e32 v5, v56
	s_waitcnt vmcnt(63) expcnt(7) lgkmcnt(15)
	s_barrier
	s_branch .LBB0_1380

.LBB0_1380:
	s_waitcnt vmcnt(16) lgkmcnt(0)
	s_mov_b32 s60, s96
	s_mov_b32 s61, s97
	s_mov_b64 s[66:67], s[98:99]
	s_mov_b64 s[68:69], s[96:97]
	s_mov_b64 s[70:71], s[98:99]
	s_movk_i32 s72, 0x1000
	s_movk_i32 s73, 0x3fff
	s_movk_i32 s74, 0x2000
	s_movk_i32 s75, 0x3000
	s_mov_b32 s76, 0xf800000
	s_mov_b32 s77, 0x8080808
	s_mov_b32 s78, 0x400000
	s_mov_b32 s79, 0x800000
	s_mov_b32 s80, 0xc00000
	s_mov_b32 s81, 0x1000000
	v_cmp_eq_u32_e64 s[82:83], 0, v246
	s_mov_b64 s[86:87], 0
	v_mul_f32_e32 v202, v207, v207
	v_mul_f32_e32 v203, v209, v209
	v_max_f32_e64 v204, |v207|, |v207|
	v_max_f32_e64 v205, |v206|, |v206|
	v_max_f32_e64 v214, |v209|, |v209|
	v_max_f32_e64 v215, |v208|, |v208|
	s_nop 0
	v_mul_f32_e32 v216, v191, v191
	v_mul_f32_e32 v217, v193, v193
	s_nop 0
	v_mul_f32_e32 v229, v187, v187
	v_mul_f32_e32 v235, v189, v189
	v_fmac_f32_e32 v202, v206, v206
	v_fmac_f32_e32 v203, v208, v208
	v_max_f32_e32 v204, v205, v204
	v_max_f32_e32 v205, v215, v214
	v_fmac_f32_e32 v216, v190, v190
	v_fmac_f32_e32 v217, v192, v192
	v_max_f32_e64 v218, |v191|, |v191|
	v_max_f32_e64 v219, |v190|, |v190|
	v_max_f32_e64 v236, |v187|, |v187|
	v_max_f32_e64 v237, |v186|, |v186|
	s_nop 0
	v_mul_f32_e32 v240, v179, v179
	v_mul_f32_e32 v241, v181, v181
	v_fmac_f32_e32 v229, v186, v186
	v_fmac_f32_e32 v235, v188, v188
	v_add_f32_e32 v202, v202, v203
	v_max3_f32 v203, v204, 0, v205
	v_add_f32_e32 v204, v216, v217
	v_max_f32_e32 v214, v219, v218
	v_max_f32_e32 v218, v237, v236
	v_fmac_f32_e32 v240, v178, v178
	v_fmac_f32_e32 v241, v180, v180
	s_nop 0
	v_mul_f32_e32 v236, v183, v183
	v_mul_f32_e32 v237, v185, v185
	v_add_f32_e32 v205, v229, v235
	v_add_f32_e32 v202, v202, v204
	v_max_f32_e64 v220, |v193|, |v193|
	v_max_f32_e64 v221, |v192|, |v192|
	v_add_f32_e32 v216, v240, v241
	v_fmac_f32_e32 v236, v182, v182
	v_fmac_f32_e32 v237, v184, v184
	v_add_f32_e32 v202, v202, v205
	v_max_f32_e64 v238, |v189|, |v189|
	v_max_f32_e64 v239, |v188|, |v188|
	v_max_f32_e32 v215, v221, v220
	v_add_f32_e32 v202, v202, v216
	v_add_f32_e32 v204, v236, v237
	v_max_f32_e64 v242, |v179|, |v179|
	v_max_f32_e64 v243, |v178|, |v178|
	v_max_f32_e64 v244, |v181|, |v181|
	v_max_f32_e64 v245, |v180|, |v180|
	v_max_f32_e32 v219, v239, v238
	v_max3_f32 v203, v203, v214, v215
	v_add_f32_e32 v202, v202, v204
	v_max_f32_e64 v204, |v183|, |v183|
	v_max_f32_e64 v205, |v182|, |v182|
	v_max_f32_e32 v220, v243, v242
	v_max_f32_e32 v221, v245, v244
	v_max3_f32 v203, v203, v218, v219
	v_max_f32_e32 v204, v205, v204
	v_max_f32_e64 v205, |v185|, |v185|
	v_max_f32_e64 v214, |v184|, |v184|
	v_max3_f32 v203, v203, v220, v221
	v_max_f32_e32 v205, v214, v205
	v_max3_f32 v203, v203, v204, v205
	v_mov_b32_e32 v218, v136
	v_mov_b32_e32 v219, v137
	v_mov_b32_e32 v220, v138
	v_mov_b32_e32 v221, v139
	v_mov_b32_e32 v214, v140
	v_mov_b32_e32 v215, v141
	v_mov_b32_e32 v216, v142
	v_mov_b32_e32 v217, v143
	v_cmp_lt_i32_e32 vcc, v250, v247
	s_nop 0
	v_mul_f32_e32 v204, v171, v171
	v_mul_f32_e32 v194, v173, v173
	v_fmac_f32_e32 v204, v170, v170
	v_fmac_f32_e32 v194, v172, v172
	v_add_f32_e32 v194, v204, v194
	v_add_f32_e32 v194, v202, v194
	v_max_f32_e64 v195, |v171|, |v171|
	v_max_f32_e64 v202, |v170|, |v170|
	v_max_f32_e32 v195, v202, v195
	v_max_f32_e64 v202, |v173|, |v173|
	v_max_f32_e64 v204, |v172|, |v172|
	v_max_f32_e32 v202, v204, v202
	v_max3_f32 v195, v203, v195, v202
	s_nop 0
	v_mul_f32_e32 v202, v223, v223
	v_mul_f32_e32 v203, v225, v225
	v_fmac_f32_e32 v202, v222, v222
	v_fmac_f32_e32 v203, v224, v224
	v_add_f32_e32 v202, v202, v203
	v_add_f32_e32 v194, v194, v202
	v_max_f32_e64 v202, |v223|, |v223|
	v_max_f32_e64 v203, |v222|, |v222|
	v_max_f32_e32 v202, v203, v202
	v_max_f32_e64 v203, |v225|, |v225|
	v_max_f32_e64 v204, |v224|, |v224|
	v_max_f32_e32 v203, v204, v203
	v_max3_f32 v229, v195, v202, v203
	v_mov_b32_e32 v202, v144
	v_mov_b32_e32 v203, v145
	v_mov_b32_e32 v204, v146
	v_mov_b32_e32 v205, v147
	s_nop 0
	v_mul_f32_e32 v195, v211, v211
	v_mul_f32_e32 v235, v213, v213
	v_fmac_f32_e32 v195, v210, v210
	v_fmac_f32_e32 v235, v212, v212
	v_add_f32_e32 v195, v195, v235
	v_add_f32_e32 v235, v194, v195
	v_max_f32_e64 v194, |v211|, |v211|
	v_max_f32_e64 v195, |v210|, |v210|
	v_max_f32_e32 v236, v195, v194
	v_max_f32_e64 v194, |v213|, |v213|
	v_max_f32_e64 v195, |v212|, |v212|
	v_max_f32_e32 v237, v195, v194
	v_mov_b32_e32 v194, v148
	v_mov_b32_e32 v195, v149
	v_mov_b32_e32 v196, v150
	v_mov_b32_e32 v197, v151
	v_max3_f32 v229, v229, v236, v237
	s_nop 0
	v_mul_f32_e32 v236, v199, v199
	v_mul_f32_e32 v237, v201, v201
	v_fmac_f32_e32 v236, v198, v198
	v_fmac_f32_e32 v237, v200, v200
	v_add_f32_e32 v236, v236, v237
	v_add_f32_e32 v235, v235, v236
	v_max_f32_e64 v236, |v199|, |v199|
	v_max_f32_e64 v237, |v198|, |v198|
	v_max_f32_e32 v236, v237, v236
	v_max_f32_e64 v237, |v201|, |v201|
	v_max_f32_e64 v238, |v200|, |v200|
	v_max_f32_e32 v237, v238, v237
	v_max3_f32 v229, v229, v236, v237
	s_nop 0
	v_mul_f32_e32 v236, v175, v175
	v_mul_f32_e32 v237, v177, v177
	v_fmac_f32_e32 v236, v174, v174
	v_fmac_f32_e32 v237, v176, v176
	v_add_f32_e32 v236, v236, v237
	v_add_f32_e32 v235, v235, v236
	v_max_f32_e64 v236, |v175|, |v175|
	v_max_f32_e64 v237, |v174|, |v174|
	v_max_f32_e32 v236, v237, v236
	v_max_f32_e64 v237, |v177|, |v177|
	v_max_f32_e64 v238, |v176|, |v176|
	v_max_f32_e32 v237, v238, v237
	v_max3_f32 v229, v229, v236, v237
	s_nop 0
	v_mul_f32_e32 v236, v167, v167
	v_mul_f32_e32 v237, v169, v169
	v_fmac_f32_e32 v236, v166, v166
	v_fmac_f32_e32 v237, v168, v168
	v_add_f32_e32 v236, v236, v237
	v_add_f32_e32 v235, v235, v236
	v_max_f32_e64 v236, |v167|, |v167|
	v_max_f32_e64 v237, |v166|, |v166|
	v_max_f32_e32 v236, v237, v236
	v_max_f32_e64 v237, |v169|, |v169|
	v_max_f32_e64 v238, |v168|, |v168|
	v_max_f32_e32 v237, v238, v237
	v_max3_f32 v229, v229, v236, v237
	s_nop 0
	v_mul_f32_e32 v236, v219, v219
	v_mul_f32_e32 v237, v221, v221
	v_fmac_f32_e32 v236, v218, v218
	v_fmac_f32_e32 v237, v220, v220
	v_add_f32_e32 v236, v236, v237
	v_add_f32_e32 v235, v235, v236
	v_max_f32_e64 v236, |v219|, |v219|
	v_max_f32_e64 v237, |v218|, |v218|
	v_max_f32_e32 v236, v237, v236
	v_max_f32_e64 v237, |v221|, |v221|
	v_max_f32_e64 v238, |v220|, |v220|
	v_max_f32_e32 v237, v238, v237
	v_max3_f32 v229, v229, v236, v237
	s_nop 0
	v_mul_f32_e32 v236, v215, v215
	v_mul_f32_e32 v237, v217, v217
	v_fmac_f32_e32 v236, v214, v214
	v_fmac_f32_e32 v237, v216, v216
	v_add_f32_e32 v236, v236, v237
	v_add_f32_e32 v235, v235, v236
	v_max_f32_e64 v236, |v215|, |v215|
	v_max_f32_e64 v237, |v214|, |v214|
	v_max_f32_e32 v236, v237, v236
	v_max_f32_e64 v237, |v217|, |v217|
	v_max_f32_e64 v238, |v216|, |v216|
	v_max_f32_e32 v237, v238, v237
	v_max3_f32 v229, v229, v236, v237
	s_nop 0
	v_mul_f32_e32 v236, v203, v203
	v_mul_f32_e32 v237, v205, v205
	v_fmac_f32_e32 v236, v202, v202
	v_fmac_f32_e32 v237, v204, v204
	v_add_f32_e32 v236, v236, v237
	v_add_f32_e32 v235, v235, v236
	v_max_f32_e64 v236, |v203|, |v203|
	v_max_f32_e64 v237, |v202|, |v202|
	v_max_f32_e32 v236, v237, v236
	v_max_f32_e64 v237, |v205|, |v205|
	v_max_f32_e64 v238, |v204|, |v204|
	v_max_f32_e32 v237, v238, v237
	v_max3_f32 v229, v229, v236, v237
	s_nop 0
	v_mul_f32_e32 v236, v195, v195
	v_mul_f32_e32 v237, v197, v197
	v_fmac_f32_e32 v236, v194, v194
	v_fmac_f32_e32 v237, v196, v196
	v_add_f32_e32 v236, v236, v237
	v_add_f32_e32 v235, v235, v236
	v_max_f32_e64 v236, |v195|, |v195|
	v_max_f32_e64 v237, |v194|, |v194|
	v_max_f32_e32 v236, v237, v236
	v_max_f32_e64 v237, |v197|, |v197|
	v_max_f32_e64 v238, |v196|, |v196|
	v_max_f32_e32 v237, v238, v237
	v_max3_f32 v229, v229, v236, v237
	v_mul_f32_e32 v236, v163, v163
	v_mul_f32_e32 v237, v165, v165
	v_fmac_f32_e32 v236, v162, v162
	v_fmac_f32_e32 v237, v164, v164
	v_add_f32_e32 v236, v236, v237
	v_add_f32_e32 v235, v235, v236
	v_max_f32_e64 v236, |v163|, |v163|
	v_max_f32_e64 v237, |v162|, |v162|
	v_max_f32_e32 v236, v237, v236
	v_max_f32_e64 v237, |v165|, |v165|
	v_max_f32_e64 v240, |v164|, |v164|
	v_cndmask_b32_e32 v238, v246, v250, vcc
	v_max_f32_e32 v237, v240, v237
	v_lshlrev_b32_e32 v238, 2, v238
	v_max3_f32 v229, v229, v236, v237
	ds_bpermute_b32 v239, v238, v235
	ds_bpermute_b32 v236, v238, v229
	v_cmp_lt_i32_e32 vcc, v251, v247
	s_waitcnt lgkmcnt(1)
	v_add_f32_e32 v235, v235, v239
	v_cndmask_b32_e32 v237, v246, v251, vcc
	v_lshlrev_b32_e32 v237, 2, v237
	s_waitcnt lgkmcnt(0)
	v_max_f32_e32 v236, v236, v236
	ds_bpermute_b32 v238, v237, v235
	v_max_f32_e32 v229, v229, v236
	ds_bpermute_b32 v236, v237, v229
	v_cmp_lt_i32_e32 vcc, v252, v247
	s_waitcnt lgkmcnt(1)
	v_add_f32_e32 v235, v235, v238
	v_cndmask_b32_e32 v237, v246, v252, vcc
	v_lshlrev_b32_e32 v237, 2, v237
	ds_bpermute_b32 v238, v237, v235
	s_waitcnt lgkmcnt(1)
	v_max_f32_e32 v236, v236, v236
	v_max_f32_e32 v229, v229, v236
	ds_bpermute_b32 v236, v237, v229
	v_cmp_lt_i32_e32 vcc, v253, v247
	s_waitcnt lgkmcnt(1)
	v_add_f32_e32 v235, v235, v238
	s_waitcnt lgkmcnt(0)
	v_max_f32_e32 v236, v236, v236
	v_cndmask_b32_e32 v237, v246, v253, vcc
	v_lshlrev_b32_e32 v237, 2, v237
	ds_bpermute_b32 v238, v237, v235
	v_max_f32_e32 v229, v229, v236
	ds_bpermute_b32 v236, v237, v229
	v_cmp_lt_i32_e32 vcc, v249, v247
	s_waitcnt lgkmcnt(1)
	v_add_f32_e32 v235, v235, v238
	v_cndmask_b32_e32 v237, v246, v249, vcc
	v_lshlrev_b32_e32 v237, 2, v237
	ds_bpermute_b32 v238, v237, v235
	s_waitcnt lgkmcnt(1)
	v_max_f32_e32 v236, v236, v236
	v_max_f32_e32 v229, v229, v236
	v_cmp_lt_i32_e32 vcc, v248, v247
	ds_bpermute_b32 v236, v237, v229
	s_waitcnt lgkmcnt(1)
	v_add_f32_e32 v235, v235, v238
	v_cndmask_b32_e32 v237, v246, v248, vcc
	v_lshlrev_b32_e32 v237, 2, v237
	ds_bpermute_b32 v238, v237, v235
	s_waitcnt lgkmcnt(1)
	v_max_f32_e32 v236, v236, v236
	v_max_f32_e32 v229, v229, v236
	ds_bpermute_b32 v236, v237, v229
	s_waitcnt lgkmcnt(1)
	v_add_f32_e32 v235, v235, v238
	v_mul_f32_e32 v235, 0x39800000, v235
	v_mul_f32_e32 v237, 0x4f800000, v235
	v_cmp_gt_f32_e32 vcc, s76, v235
	s_waitcnt lgkmcnt(0)
	v_max_f32_e32 v236, v236, v236
	v_max_f32_e32 v229, v229, v236
	v_cndmask_b32_e32 v235, v235, v237, vcc
	v_sqrt_f32_e32 v237, v235
	v_mul_f32_e32 v229, 0x3e088889, v229
	v_add_u32_e32 v236, -1, v237
	v_fma_f32 v238, -v236, v237, v235
	v_cmp_ge_f32_e64 s[88:89], 0, v238
	v_add_u32_e32 v238, 1, v237
	s_nop 0
	v_cndmask_b32_e64 v236, v237, v236, s[88:89]
	v_fma_f32 v237, -v238, v237, v235
	v_cmp_lt_f32_e64 s[88:89], 0, v237
	s_nop 1
	v_cndmask_b32_e64 v236, v236, v238, s[88:89]
	v_mul_f32_e32 v237, 0x37800000, v236
	v_cndmask_b32_e32 v236, v236, v237, vcc
	v_cmp_class_f32_e32 vcc, v235, v233
	s_nop 1
	v_cndmask_b32_e32 v235, v236, v235, vcc
	v_mul_f32_e32 v235, 0x3eab9f56, v235
	v_min_f32_e32 v229, v235, v229
	v_max_f32_e32 v235, 0xda24260, v229
	v_div_scale_f32 v229, s[88:89], v235, v235, 1.0
	v_rcp_f32_e32 v236, v229
	s_nop 0
	v_fma_f32 v237, -v229, v236, 1.0
	v_fmac_f32_e32 v236, v237, v236
	v_div_scale_f32 v237, vcc, 1.0, v235, 1.0
	v_mul_f32_e32 v238, v237, v236
	v_fma_f32 v239, -v229, v238, v237
	v_fmac_f32_e32 v238, v239, v236
	v_fma_f32 v229, -v229, v238, v237
	v_div_fmas_f32 v229, v229, v236, v238
	v_div_fixup_f32 v229, v229, v235, 1.0
	v_mul_f32_e32 v179, v179, v229
	v_mul_f32_e32 v178, v178, v229
	v_floor_f32_e32 v179, v179
	v_mul_f32_e32 v180, v180, v229
	v_floor_f32_e32 v178, v178
	v_add_f32_e32 v179, 0x41000000, v179
	v_floor_f32_e32 v180, v180
	v_add_f32_e32 v178, 0x41000000, v178
	v_med3_f32 v179, v179, 0, v234
	v_add_f32_e32 v180, 0x41000000, v180
	v_med3_f32 v178, v178, 0, v234
	v_cvt_i32_f32_e32 v179, v179
	v_med3_f32 v180, v180, 0, v234
	v_cvt_i32_f32_e32 v178, v178
	v_cvt_i32_f32_sdwa v180, v180 dst_sel:WORD_1 dst_unused:UNUSED_PAD src0_sel:DWORD
	v_lshlrev_b32_e32 v179, 8, v179
	v_mul_f32_e32 v171, v171, v229
	v_mul_f32_e32 v170, v170, v229
	v_or3_b32 v178, v179, v178, v180
	v_mul_f32_e32 v179, v181, v229
	v_mul_f32_e32 v181, v183, v229
	v_floor_f32_e32 v179, v179
	v_mul_f32_e32 v180, v182, v229
	v_floor_f32_e32 v181, v181
	v_mul_f32_e32 v182, v184, v229
	v_add_f32_e32 v179, 0x41000000, v179
	v_floor_f32_e32 v180, v180
	v_add_f32_e32 v181, 0x41000000, v181
	v_floor_f32_e32 v182, v182
	v_mul_f32_e32 v183, v185, v229
	v_floor_f32_e32 v171, v171
	v_mul_f32_e32 v172, v172, v229
	v_med3_f32 v179, v179, 0, v234
	v_add_f32_e32 v180, 0x41000000, v180
	v_med3_f32 v181, v181, 0, v234
	v_add_f32_e32 v182, 0x41000000, v182
	v_floor_f32_e32 v183, v183
	v_floor_f32_e32 v170, v170
	v_add_f32_e32 v171, 0x41000000, v171
	v_floor_f32_e32 v172, v172
	v_mul_f32_e32 v175, v175, v229
	v_cvt_i32_f32_sdwa v179, v179 dst_sel:BYTE_3 dst_unused:UNUSED_PAD src0_sel:DWORD
	v_med3_f32 v180, v180, 0, v234
	v_cvt_i32_f32_e32 v181, v181
	v_med3_f32 v182, v182, 0, v234
	v_add_f32_e32 v183, 0x41000000, v183
	v_add_f32_e32 v170, 0x41000000, v170
	v_med3_f32 v171, v171, 0, v234
	v_add_f32_e32 v172, 0x41000000, v172
	v_mul_f32_e32 v174, v174, v229
	v_floor_f32_e32 v175, v175
	v_mul_f32_e32 v176, v176, v229
	v_cvt_i32_f32_e32 v180, v180
	v_cvt_i32_f32_sdwa v182, v182 dst_sel:WORD_1 dst_unused:UNUSED_PAD src0_sel:DWORD
	v_med3_f32 v183, v183, 0, v234
	v_med3_f32 v170, v170, 0, v234
	v_cvt_i32_f32_e32 v171, v171
	v_med3_f32 v172, v172, 0, v234
	v_floor_f32_e32 v174, v174
	v_add_f32_e32 v175, 0x41000000, v175
	v_floor_f32_e32 v176, v176
	v_cvt_i32_f32_sdwa v183, v183 dst_sel:BYTE_3 dst_unused:UNUSED_PAD src0_sel:DWORD
	v_cvt_i32_f32_e32 v170, v170
	v_cvt_i32_f32_sdwa v172, v172 dst_sel:WORD_1 dst_unused:UNUSED_PAD src0_sel:DWORD
	v_add_f32_e32 v174, 0x41000000, v174
	v_med3_f32 v175, v175, 0, v234
	v_add_f32_e32 v176, 0x41000000, v176
	v_med3_f32 v174, v174, 0, v234
	v_cvt_i32_f32_e32 v175, v175
	v_med3_f32 v176, v176, 0, v234
	v_bitop3_b32 v178, v178, s77, v179 bitop3:0x36
	v_lshlrev_b32_e32 v179, 8, v181
	v_cvt_i32_f32_e32 v174, v174
	v_cvt_i32_f32_sdwa v176, v176 dst_sel:WORD_1 dst_unused:UNUSED_PAD src0_sel:DWORD
	v_or3_b32 v179, v179, v180, v182
	v_lshlrev_b32_e32 v171, 8, v171
	v_or_b32_e32 v180, v179, v183
	v_bitop3_b32 v179, v179, s77, v183 bitop3:0x36
	v_or3_b32 v170, v171, v170, v172
	v_mul_f32_e32 v171, v173, v229
	v_mul_f32_e32 v173, v223, v229
	v_cndmask_b32_e64 v179, v179, v180, s[86:87]
	v_floor_f32_e32 v171, v171
	v_mul_f32_e32 v172, v222, v229
	v_floor_f32_e32 v173, v173
	v_mul_f32_e32 v180, v224, v229
	v_lshlrev_b32_e32 v175, 8, v175
	v_add_f32_e32 v171, 0x41000000, v171
	v_floor_f32_e32 v172, v172
	v_add_f32_e32 v173, 0x41000000, v173
	v_floor_f32_e32 v180, v180
	v_or3_b32 v174, v175, v174, v176
	v_mul_f32_e32 v175, v177, v229
	v_mul_f32_e32 v167, v167, v229
	v_med3_f32 v171, v171, 0, v234
	v_add_f32_e32 v172, 0x41000000, v172
	v_med3_f32 v173, v173, 0, v234
	v_add_f32_e32 v180, 0x41000000, v180
	v_floor_f32_e32 v175, v175
	v_mul_f32_e32 v166, v166, v229
	v_floor_f32_e32 v167, v167
	v_mul_f32_e32 v168, v168, v229
	v_cvt_i32_f32_sdwa v171, v171 dst_sel:BYTE_3 dst_unused:UNUSED_PAD src0_sel:DWORD
	v_med3_f32 v172, v172, 0, v234
	v_cvt_i32_f32_e32 v173, v173
	v_med3_f32 v180, v180, 0, v234
	v_add_f32_e32 v175, 0x41000000, v175
	v_floor_f32_e32 v166, v166
	v_add_f32_e32 v167, 0x41000000, v167
	v_floor_f32_e32 v168, v168
	v_cvt_i32_f32_e32 v172, v172
	v_cvt_i32_f32_sdwa v180, v180 dst_sel:WORD_1 dst_unused:UNUSED_PAD src0_sel:DWORD
	v_med3_f32 v175, v175, 0, v234
	v_add_f32_e32 v166, 0x41000000, v166
	v_med3_f32 v167, v167, 0, v234
	v_add_f32_e32 v168, 0x41000000, v168
	v_cvt_i32_f32_sdwa v175, v175 dst_sel:BYTE_3 dst_unused:UNUSED_PAD src0_sel:DWORD
	v_med3_f32 v166, v166, 0, v234
	v_cvt_i32_f32_e32 v167, v167
	v_med3_f32 v168, v168, 0, v234
	v_cvt_i32_f32_e32 v166, v166
	v_cvt_i32_f32_sdwa v168, v168 dst_sel:WORD_1 dst_unused:UNUSED_PAD src0_sel:DWORD
	v_mul_f32_e32 v181, v225, v229
	v_bitop3_b32 v170, v170, s77, v171 bitop3:0x36
	v_lshlrev_b32_e32 v171, 8, v173
	v_floor_f32_e32 v181, v181
	v_or3_b32 v171, v171, v172, v180
	v_mul_f32_e32 v180, v211, v229
	v_mul_f32_e32 v169, v169, v229
	v_add_f32_e32 v181, 0x41000000, v181
	v_mul_f32_e32 v173, v210, v229
	v_floor_f32_e32 v180, v180
	v_mul_f32_e32 v182, v212, v229
	v_floor_f32_e32 v169, v169
	v_bitop3_b32 v174, v174, s77, v175 bitop3:0x36
	v_lshlrev_b32_e32 v167, 8, v167
	v_mul_f32_e32 v175, v219, v229
	v_med3_f32 v181, v181, 0, v234
	v_floor_f32_e32 v173, v173
	v_add_f32_e32 v180, 0x41000000, v180
	v_floor_f32_e32 v182, v182
	v_add_f32_e32 v169, 0x41000000, v169
	v_or3_b32 v166, v167, v166, v168
	v_mul_f32_e32 v168, v218, v229
	v_floor_f32_e32 v175, v175
	v_mul_f32_e32 v176, v220, v229
	v_cvt_i32_f32_sdwa v181, v181 dst_sel:BYTE_3 dst_unused:UNUSED_PAD src0_sel:DWORD
	v_add_f32_e32 v173, 0x41000000, v173
	v_med3_f32 v180, v180, 0, v234
	v_add_f32_e32 v182, 0x41000000, v182
	v_med3_f32 v169, v169, 0, v234
	v_floor_f32_e32 v168, v168
	v_add_f32_e32 v175, 0x41000000, v175
	v_floor_f32_e32 v176, v176
	v_med3_f32 v173, v173, 0, v234
	v_cvt_i32_f32_e32 v180, v180
	v_med3_f32 v182, v182, 0, v234
	v_cvt_i32_f32_sdwa v169, v169 dst_sel:BYTE_3 dst_unused:UNUSED_PAD src0_sel:DWORD
	v_add_f32_e32 v168, 0x41000000, v168
	v_med3_f32 v175, v175, 0, v234
	v_add_f32_e32 v176, 0x41000000, v176
	v_cvt_i32_f32_e32 v173, v173
	v_cvt_i32_f32_sdwa v182, v182 dst_sel:WORD_1 dst_unused:UNUSED_PAD src0_sel:DWORD
	v_med3_f32 v168, v168, 0, v234
	v_cvt_i32_f32_e32 v175, v175
	v_med3_f32 v176, v176, 0, v234
	v_cvt_i32_f32_e32 v168, v168
	v_cvt_i32_f32_sdwa v176, v176 dst_sel:WORD_1 dst_unused:UNUSED_PAD src0_sel:DWORD
	v_or_b32_e32 v172, v171, v181
	v_bitop3_b32 v171, v171, s77, v181 bitop3:0x36
	v_cndmask_b32_e64 v171, v171, v172, s[86:87]
	v_lshlrev_b32_e32 v172, 8, v180
	v_or_b32_e32 v167, v166, v169
	v_bitop3_b32 v166, v166, s77, v169 bitop3:0x36
	v_or3_b32 v172, v172, v173, v182
	v_mul_f32_e32 v173, v213, v229
	v_mul_f32_e32 v181, v199, v229
	v_cndmask_b32_e64 v166, v166, v167, s[86:87]
	v_lshlrev_b32_e32 v167, 8, v175
	v_floor_f32_e32 v173, v173
	v_mul_f32_e32 v180, v198, v229
	v_floor_f32_e32 v181, v181
	v_mul_f32_e32 v182, v200, v229
	v_or3_b32 v167, v167, v168, v176
	v_mul_f32_e32 v168, v221, v229
	v_mul_f32_e32 v175, v215, v229
	v_add_f32_e32 v173, 0x41000000, v173
	v_floor_f32_e32 v180, v180
	v_add_f32_e32 v181, 0x41000000, v181
	v_floor_f32_e32 v182, v182
	v_mul_f32_e32 v183, v201, v229
	v_floor_f32_e32 v168, v168
	v_mul_f32_e32 v169, v214, v229
	v_floor_f32_e32 v175, v175
	v_mul_f32_e32 v176, v216, v229
	v_med3_f32 v173, v173, 0, v234
	v_add_f32_e32 v180, 0x41000000, v180
	v_med3_f32 v181, v181, 0, v234
	v_add_f32_e32 v182, 0x41000000, v182
	v_floor_f32_e32 v183, v183
	v_add_f32_e32 v168, 0x41000000, v168
	v_floor_f32_e32 v169, v169
	v_add_f32_e32 v175, 0x41000000, v175
	v_floor_f32_e32 v176, v176
	v_cvt_i32_f32_sdwa v173, v173 dst_sel:BYTE_3 dst_unused:UNUSED_PAD src0_sel:DWORD
	v_med3_f32 v180, v180, 0, v234
	v_cvt_i32_f32_e32 v181, v181
	v_med3_f32 v182, v182, 0, v234
	v_add_f32_e32 v183, 0x41000000, v183
	v_med3_f32 v168, v168, 0, v234
	v_add_f32_e32 v169, 0x41000000, v169
	v_med3_f32 v175, v175, 0, v234
	v_add_f32_e32 v176, 0x41000000, v176
	v_cvt_i32_f32_e32 v180, v180
	v_cvt_i32_f32_sdwa v182, v182 dst_sel:WORD_1 dst_unused:UNUSED_PAD src0_sel:DWORD
	v_med3_f32 v183, v183, 0, v234
	v_cvt_i32_f32_sdwa v168, v168 dst_sel:BYTE_3 dst_unused:UNUSED_PAD src0_sel:DWORD
	v_med3_f32 v169, v169, 0, v234
	v_cvt_i32_f32_e32 v175, v175
	v_med3_f32 v176, v176, 0, v234
	v_cvt_i32_f32_sdwa v183, v183 dst_sel:BYTE_3 dst_unused:UNUSED_PAD src0_sel:DWORD
	v_cvt_i32_f32_e32 v169, v169
	v_cvt_i32_f32_sdwa v176, v176 dst_sel:WORD_1 dst_unused:UNUSED_PAD src0_sel:DWORD
	v_bitop3_b32 v172, v172, s77, v173 bitop3:0x36
	v_lshlrev_b32_e32 v173, 8, v181
	v_or3_b32 v173, v173, v180, v182
	v_mul_f32_e32 v177, v217, v229
	v_bitop3_b32 v167, v167, s77, v168 bitop3:0x36
	v_lshlrev_b32_e32 v168, 8, v175
	v_or_b32_e32 v180, v173, v183
	v_bitop3_b32 v173, v173, s77, v183 bitop3:0x36
	v_floor_f32_e32 v177, v177
	v_or3_b32 v168, v168, v169, v176
	v_mul_f32_e32 v176, v203, v229
	v_cndmask_b32_e64 v173, v173, v180, s[86:87]
	v_add_f32_e32 v177, 0x41000000, v177
	v_mul_f32_e32 v175, v202, v229
	v_floor_f32_e32 v176, v176
	v_mul_f32_e32 v180, v204, v229
	v_med3_f32 v177, v177, 0, v234
	v_floor_f32_e32 v175, v175
	v_add_f32_e32 v176, 0x41000000, v176
	v_floor_f32_e32 v180, v180
	v_cvt_i32_f32_sdwa v177, v177 dst_sel:BYTE_3 dst_unused:UNUSED_PAD src0_sel:DWORD
	v_add_f32_e32 v175, 0x41000000, v175
	v_med3_f32 v176, v176, 0, v234
	v_add_f32_e32 v180, 0x41000000, v180
	v_med3_f32 v175, v175, 0, v234
	v_cvt_i32_f32_e32 v176, v176
	v_med3_f32 v180, v180, 0, v234
	v_cvt_i32_f32_e32 v175, v175
	v_cvt_i32_f32_sdwa v180, v180 dst_sel:WORD_1 dst_unused:UNUSED_PAD src0_sel:DWORD
	v_mul_f32_e32 v191, v191, v229
	v_mul_f32_e32 v190, v190, v229
	v_floor_f32_e32 v191, v191
	v_mul_f32_e32 v192, v192, v229
	v_or_b32_e32 v169, v168, v177
	v_bitop3_b32 v168, v168, s77, v177 bitop3:0x36
	v_floor_f32_e32 v190, v190
	v_add_f32_e32 v191, 0x41000000, v191
	v_floor_f32_e32 v192, v192
	v_cndmask_b32_e64 v168, v168, v169, s[86:87]
	v_lshlrev_b32_e32 v169, 8, v176
	v_add_f32_e32 v190, 0x41000000, v190
	v_med3_f32 v191, v191, 0, v234
	v_add_f32_e32 v192, 0x41000000, v192
	v_or3_b32 v169, v169, v175, v180
	v_mul_f32_e32 v175, v205, v229
	v_mul_f32_e32 v177, v195, v229
	v_med3_f32 v190, v190, 0, v234
	v_cvt_i32_f32_e32 v191, v191
	v_med3_f32 v192, v192, 0, v234
	v_floor_f32_e32 v175, v175
	v_mul_f32_e32 v176, v194, v229
	v_floor_f32_e32 v177, v177
	v_mul_f32_e32 v180, v196, v229
	v_mul_f32_e32 v163, v163, v229
	v_cvt_i32_f32_e32 v190, v190
	v_cvt_i32_f32_sdwa v192, v192 dst_sel:WORD_1 dst_unused:UNUSED_PAD src0_sel:DWORD
	v_add_f32_e32 v175, 0x41000000, v175
	v_floor_f32_e32 v176, v176
	v_add_f32_e32 v177, 0x41000000, v177
	v_floor_f32_e32 v180, v180
	v_mul_f32_e32 v181, v197, v229
	v_mul_f32_e32 v162, v162, v229
	v_floor_f32_e32 v163, v163
	v_mul_f32_e32 v164, v164, v229
	v_mul_f32_e32 v207, v207, v229
	v_med3_f32 v175, v175, 0, v234
	v_add_f32_e32 v176, 0x41000000, v176
	v_med3_f32 v177, v177, 0, v234
	v_add_f32_e32 v180, 0x41000000, v180
	v_floor_f32_e32 v181, v181
	v_floor_f32_e32 v162, v162
	v_add_f32_e32 v163, 0x41000000, v163
	v_floor_f32_e32 v164, v164
	v_mul_f32_e32 v165, v165, v229
	v_mul_f32_e32 v206, v206, v229
	v_floor_f32_e32 v207, v207
	v_mul_f32_e32 v208, v208, v229
	v_cvt_i32_f32_sdwa v175, v175 dst_sel:BYTE_3 dst_unused:UNUSED_PAD src0_sel:DWORD
	v_med3_f32 v176, v176, 0, v234
	v_cvt_i32_f32_e32 v177, v177
	v_med3_f32 v180, v180, 0, v234
	v_add_f32_e32 v181, 0x41000000, v181
	v_add_f32_e32 v162, 0x41000000, v162
	v_med3_f32 v163, v163, 0, v234
	v_add_f32_e32 v164, 0x41000000, v164
	v_floor_f32_e32 v165, v165
	v_floor_f32_e32 v206, v206
	v_add_f32_e32 v207, 0x41000000, v207
	v_floor_f32_e32 v208, v208
	v_mul_f32_e32 v209, v209, v229
	v_lshlrev_b32_e32 v191, 8, v191
	v_mul_f32_e32 v187, v187, v229
	v_cvt_i32_f32_e32 v176, v176
	v_cvt_i32_f32_sdwa v180, v180 dst_sel:WORD_1 dst_unused:UNUSED_PAD src0_sel:DWORD
	v_med3_f32 v181, v181, 0, v234
	v_med3_f32 v162, v162, 0, v234
	v_cvt_i32_f32_e32 v163, v163
	v_med3_f32 v164, v164, 0, v234
	v_add_f32_e32 v165, 0x41000000, v165
	v_add_f32_e32 v206, 0x41000000, v206
	v_med3_f32 v207, v207, 0, v234
	v_add_f32_e32 v208, 0x41000000, v208
	v_floor_f32_e32 v209, v209
	v_or3_b32 v190, v191, v190, v192
	v_mul_f32_e32 v191, v193, v229
	v_mul_f32_e32 v186, v186, v229
	v_floor_f32_e32 v187, v187
	v_mul_f32_e32 v188, v188, v229
	v_cvt_i32_f32_sdwa v181, v181 dst_sel:BYTE_3 dst_unused:UNUSED_PAD src0_sel:DWORD
	v_cvt_i32_f32_e32 v162, v162
	v_cvt_i32_f32_sdwa v164, v164 dst_sel:WORD_1 dst_unused:UNUSED_PAD src0_sel:DWORD
	v_med3_f32 v165, v165, 0, v234
	v_med3_f32 v206, v206, 0, v234
	v_cvt_i32_f32_e32 v207, v207
	v_med3_f32 v208, v208, 0, v234
	v_add_f32_e32 v209, 0x41000000, v209
	v_floor_f32_e32 v191, v191
	v_floor_f32_e32 v186, v186
	v_add_f32_e32 v187, 0x41000000, v187
	v_floor_f32_e32 v188, v188
	v_mul_f32_e32 v189, v189, v229
	v_cvt_i32_f32_sdwa v165, v165 dst_sel:BYTE_3 dst_unused:UNUSED_PAD src0_sel:DWORD
	v_cvt_i32_f32_e32 v206, v206
	v_cvt_i32_f32_sdwa v208, v208 dst_sel:WORD_1 dst_unused:UNUSED_PAD src0_sel:DWORD
	v_med3_f32 v209, v209, 0, v234
	v_add_f32_e32 v191, 0x41000000, v191
	v_add_f32_e32 v186, 0x41000000, v186
	v_med3_f32 v187, v187, 0, v234
	v_add_f32_e32 v188, 0x41000000, v188
	v_floor_f32_e32 v189, v189
	v_bitop3_b32 v169, v169, s77, v175 bitop3:0x36
	v_lshlrev_b32_e32 v175, 8, v177
	v_cvt_i32_f32_sdwa v209, v209 dst_sel:BYTE_3 dst_unused:UNUSED_PAD src0_sel:DWORD
	v_med3_f32 v191, v191, 0, v234
	v_med3_f32 v186, v186, 0, v234
	v_cvt_i32_f32_e32 v187, v187
	v_med3_f32 v188, v188, 0, v234
	v_add_f32_e32 v189, 0x41000000, v189
	v_or3_b32 v175, v175, v176, v180
	v_lshlrev_b32_e32 v163, 8, v163
	v_cvt_i32_f32_sdwa v191, v191 dst_sel:BYTE_3 dst_unused:UNUSED_PAD src0_sel:DWORD
	v_cvt_i32_f32_e32 v186, v186
	v_cvt_i32_f32_sdwa v188, v188 dst_sel:WORD_1 dst_unused:UNUSED_PAD src0_sel:DWORD
	v_med3_f32 v189, v189, 0, v234
	v_or_b32_e32 v176, v175, v181
	v_bitop3_b32 v175, v175, s77, v181 bitop3:0x36
	v_or3_b32 v162, v163, v162, v164
	v_lshlrev_b32_e32 v207, 8, v207
	v_cvt_i32_f32_sdwa v189, v189 dst_sel:BYTE_3 dst_unused:UNUSED_PAD src0_sel:DWORD
	v_cndmask_b32_e64 v175, v175, v176, s[86:87]
	v_bitop3_b32 v176, v162, s77, v165 bitop3:0x36
	v_mov_b32_e32 v162, s61
	v_mov_b32_e32 v163, s69
	v_or3_b32 v206, v207, v206, v208
	v_cndmask_b32_e64 v163, v162, v163, s[86:87]
	v_mov_b32_e32 v162, s60
	v_mov_b32_e32 v164, s68
	v_or_b32_e32 v207, v206, v209
	v_bitop3_b32 v206, v206, s77, v209 bitop3:0x36
	v_lshlrev_b32_e32 v187, 8, v187
	v_cndmask_b32_e64 v162, v162, v164, s[86:87]
	v_lshlrev_b64 v[164:165], 8, v[230:231]
	v_cndmask_b32_e64 v206, v206, v207, s[86:87]
	v_bitop3_b32 v190, v190, s77, v191 bitop3:0x36
	v_or3_b32 v186, v187, v186, v188
	v_lshl_add_u64 v[162:163], v[162:163], 0, v[164:165]
	v_mov_b32_e32 v229, v227
	v_or_b32_e32 v187, v186, v189
	v_bitop3_b32 v186, v186, s77, v189 bitop3:0x36
	v_lshl_add_u64 v[162:163], v[162:163], 0, v[228:229]
	v_lshl_or_b32 v164, v190, 4, v206
	v_cndmask_b32_e64 v186, v186, v187, s[86:87]
	global_store_dword v[162:163], v164, off
	v_add_co_u32_e32 v164, vcc, s78, v162
	v_lshl_or_b32 v177, v178, 4, v186
	s_nop 0
	v_addc_co_u32_e32 v165, vcc, 0, v163, vcc
	global_store_dword v[164:165], v177, off
	v_add_co_u32_e32 v164, vcc, s79, v162
	v_lshl_or_b32 v170, v170, 4, v179
	s_nop 0
	v_addc_co_u32_e32 v165, vcc, 0, v163, vcc
	global_store_dword v[164:165], v170, off
	v_add_co_u32_e32 v164, vcc, s80, v162
	v_lshl_or_b32 v170, v172, 4, v171
	s_nop 0
	v_addc_co_u32_e32 v165, vcc, 0, v163, vcc
	global_store_dword v[164:165], v170, off
	v_add_co_u32_e32 v164, vcc, s81, v162
	v_lshl_or_b32 v170, v174, 4, v173
	s_nop 0
	v_addc_co_u32_e32 v165, vcc, 0, v163, vcc
	global_store_dword v[164:165], v170, off
	v_add_co_u32_e32 v164, vcc, 0x1400000, v162
	v_lshl_or_b32 v166, v167, 4, v166
	s_nop 0
	v_addc_co_u32_e32 v165, vcc, 0, v163, vcc
	global_store_dword v[164:165], v166, off
	v_add_co_u32_e32 v164, vcc, 0x1800000, v162
	v_lshl_or_b32 v166, v169, 4, v168
	s_nop 0
	v_addc_co_u32_e32 v165, vcc, 0, v163, vcc
	v_add_co_u32_e32 v162, vcc, 0x1c00000, v162
	global_store_dword v[164:165], v166, off
	v_lshl_or_b32 v164, v176, 4, v175
	v_addc_co_u32_e32 v163, vcc, 0, v163, vcc
	global_store_dword v[162:163], v164, off
	s_and_saveexec_b64 s[88:89], s[82:83]
	s_cbranch_execz .Luph_skip_scale
	v_mov_b32_e32 v162, s67
	v_mov_b32_e32 v163, s71
	v_cndmask_b32_e64 v163, v162, v163, s[86:87]
	v_mov_b32_e32 v162, s66
	v_mov_b32_e32 v164, s70
	v_cndmask_b32_e64 v162, v162, v164, s[86:87]
	v_lshl_add_u64 v[162:163], v[230:231], 2, v[162:163]
	global_store_dword v[162:163], v235, off
.Luph_skip_scale:
	s_or_b64 exec, exec, s[88:89]
	s_add_i32 s60, s39, 1
	s_min_u32 s60, s60, 6
	s_mul_i32 s61, s54, 7
	s_add_i32 s60, s60, s61
	v_mov_b32_e32 v162, s60
	s_mov_b64 s[62:63], s[94:95]
	s_mov_b64 s[64:65], s[94:95]
	s_movk_i32 s72, 0x1000
	s_movk_i32 s73, 0x3fff
	s_movk_i32 s74, 0x2000
	s_movk_i32 s75, 0x3000
	v_lshl_add_u32 v162, v162, 3, v232
	v_add_u32_e32 v163, 0xffffc000, v162
	v_cmp_lt_i32_e64 s[86:87], s73, v162
	v_mov_b32_e32 v164, s64
	s_nop 0
	v_cndmask_b32_e64 v230, v162, v163, s[86:87]
	v_mov_b32_e32 v162, s63
	v_mov_b32_e32 v163, s65
	v_cndmask_b32_e64 v163, v162, v163, s[86:87]
	v_mov_b32_e32 v162, s62
	v_ashrrev_i32_e32 v231, 31, v230
	v_cndmask_b32_e64 v162, v162, v164, s[86:87]
	v_lshlrev_b64 v[164:165], 14, v[230:231]
	v_lshl_add_u64 v[162:163], v[162:163], 0, v[164:165]
	v_lshl_add_u64 v[162:163], v[162:163], 0, v[226:227]
	v_add_co_u32_e32 v194, vcc, s74, v162
	global_load_dwordx4 v[206:209], v[162:163], off
	global_load_dwordx4 v[190:193], v[162:163], off offset:1024
	global_load_dwordx4 v[186:189], v[162:163], off offset:2048
	global_load_dwordx4 v[178:181], v[162:163], off offset:3072
	v_addc_co_u32_e32 v195, vcc, 0, v163, vcc
	global_load_dwordx4 v[182:185], v[194:195], off offset:-4096
	v_add_co_u32_e32 v164, vcc, s72, v162
	s_nop 0
	s_nop 0
	v_addc_co_u32_e32 v165, vcc, 0, v163, vcc
	global_load_dwordx4 v[170:173], v[164:165], off offset:1024
	v_add_co_u32_e32 v196, vcc, s75, v162
	s_nop 0
	s_nop 0
	v_addc_co_u32_e32 v197, vcc, 0, v163, vcc
	global_load_dwordx4 v[222:225], v[164:165], off offset:2048
	global_load_dwordx4 v[210:213], v[164:165], off offset:3072
	global_load_dwordx4 v[198:201], v[194:195], off
	global_load_dwordx4 v[174:177], v[194:195], off offset:1024
	global_load_dwordx4 v[166:169], v[194:195], off offset:2048
	s_nop 0
	global_load_dwordx4 v[162:165], v[196:197], off offset:3072
	global_load_dwordx4 v[136:139], v[194:195], off offset:3072
	global_load_dwordx4 v[140:143], v[196:197], off
	global_load_dwordx4 v[144:147], v[196:197], off offset:1024
	global_load_dwordx4 v[148:151], v[196:197], off offset:2048
	s_waitcnt vmcnt(39)
	v_cvt_f32_f16_e32 v117, v77
	v_cvt_f32_f16_e32 v93, v76
	v_cvt_f32_f16_sdwa v118, v77 dst_sel:DWORD dst_unused:UNUSED_PAD src0_sel:WORD_1
	v_cvt_f32_f16_sdwa v100, v76 dst_sel:DWORD dst_unused:UNUSED_PAD src0_sel:WORD_1
	s_waitcnt vmcnt(38)
	v_cvt_f32_f16_e32 v119, v78
	v_cvt_f32_f16_sdwa v116, v78 dst_sel:DWORD dst_unused:UNUSED_PAD src0_sel:WORD_1
	s_waitcnt vmcnt(37)
	v_cvt_f32_f16_e32 v115, v79
	v_cvt_f32_f16_sdwa v114, v79 dst_sel:DWORD dst_unused:UNUSED_PAD src0_sel:WORD_1
	s_waitcnt vmcnt(36)
	v_cvt_f32_f16_e32 v113, v80
	v_cvt_f32_f16_sdwa v112, v80 dst_sel:DWORD dst_unused:UNUSED_PAD src0_sel:WORD_1
	s_waitcnt vmcnt(35)
	v_cvt_f32_f16_e32 v111, v81
	v_cvt_f32_f16_sdwa v110, v81 dst_sel:DWORD dst_unused:UNUSED_PAD src0_sel:WORD_1
	v_add_f32_e32 v97, v117, v93
	v_add_f32_e32 v104, v118, v100
	s_waitcnt vmcnt(34)
	v_cvt_f32_f16_e32 v109, v82
	v_cvt_f32_f16_sdwa v108, v82 dst_sel:DWORD dst_unused:UNUSED_PAD src0_sel:WORD_1
	v_add_f32_e32 v95, v97, v119
	v_add_f32_e32 v102, v104, v116
	s_waitcnt vmcnt(33)
	v_cvt_f32_f16_e32 v107, v83
	v_cvt_f32_f16_sdwa v106, v83 dst_sel:DWORD dst_unused:UNUSED_PAD src0_sel:WORD_1
	v_add_f32_e32 v96, v95, v115
	v_add_f32_e32 v103, v102, v114
	v_add_f32_e32 v92, v96, v113
	v_add_f32_e32 v99, v103, v112
	v_add_f32_e32 v94, v92, v111
	v_add_f32_e32 v101, v99, v110
	v_add_f32_e32 v98, v94, v109
	v_add_f32_e32 v105, v101, v108
	v_add_f32_e32 v60, v98, v107
	v_add_f32_e32 v61, v105, v106
	ds_write_b64 v65, v[60:61]
	s_waitcnt lgkmcnt(0)
	s_barrier
	ds_read2st64_b64 v[46:49], v64 offset1:1
	ds_read2st64_b64 v[42:45], v64 offset0:2 offset1:3
	ds_read2st64_b64 v[38:41], v64 offset0:4 offset1:5
	ds_read2st64_b64 v[34:37], v64 offset0:6 offset1:7
	s_waitcnt lgkmcnt(3)
	v_pk_add_f32 v[62:63], v[46:47], 0 op_sel_hi:[1,0]
	s_nop 0
	v_pk_add_f32 v[46:47], v[62:63], v[48:49]
	s_waitcnt lgkmcnt(2)
	v_pk_add_f32 v[46:47], v[46:47], v[42:43]
	s_nop 0
	v_pk_add_f32 v[46:47], v[46:47], v[44:45]
	s_waitcnt lgkmcnt(1)
	v_pk_add_f32 v[46:47], v[46:47], v[38:39]
	s_nop 0
	v_pk_add_f32 v[46:47], v[46:47], v[40:41]
	s_waitcnt lgkmcnt(0)
	v_pk_add_f32 v[46:47], v[46:47], v[34:35]
	s_nop 0
	v_pk_add_f32 v[46:47], v[46:47], v[36:37]
	s_and_saveexec_b64 s[36:37], s[6:7]
	ds_write_b64 v69, v[46:47]
	s_or_b64 exec, exec, s[36:37]
	v_cndmask_b32_e64 v63, 0, v63, s[22:23]
	v_add_f32_e32 v49, v49, v63
	v_cndmask_b32_e64 v49, v63, v49, s[20:21]
	v_add_f32_e32 v43, v43, v49
	v_cndmask_b32_e64 v43, v49, v43, s[18:19]
	v_add_f32_e32 v45, v45, v43
	v_cndmask_b32_e64 v43, v43, v45, s[16:17]
	v_add_f32_e32 v39, v39, v43
	v_cndmask_b32_e64 v39, v43, v39, s[14:15]
	v_add_f32_e32 v41, v41, v39
	v_cndmask_b32_e64 v39, v39, v41, s[12:13]
	v_add_f32_e32 v35, v35, v39
	v_cndmask_b32_e64 v35, v39, v35, s[10:11]
	v_add_f32_e32 v37, v37, v35
	v_cndmask_b32_e64 v35, v35, v37, s[8:9]
	v_add_f32_e32 v37, v61, v35
	v_sub_f32_e32 v37, v47, v37
	v_mul_f32_e32 v37, 0x3fb8aa3b, v37
	v_exp_f32_e32 v131, v37
	v_add_f32_e32 v37, v105, v35
	v_sub_f32_e32 v37, v47, v37
	v_mul_f32_e32 v37, 0x3fb8aa3b, v37
	v_exp_f32_e32 v105, v37
	v_add_f32_e32 v37, v104, v35
	v_mul_f32_e32 v117, 0x3fb8aa3b, v117
	v_sub_f32_e32 v37, v47, v37
	v_exp_f32_e32 v124, v117
	v_mul_f32_e32 v117, 0x3fb8aa3b, v118
	v_mul_f32_e32 v37, 0x3fb8aa3b, v37
	v_mul_f32_e32 v120, 0x3fb8aa3b, v93
	v_mul_f32_e32 v121, 0x3fb8aa3b, v100
	v_exp_f32_e32 v118, v117
	v_mul_f32_e32 v117, 0x3fb8aa3b, v119
	v_exp_f32_e32 v132, v37
	v_add_f32_e32 v37, v35, v100
	v_exp_f32_e32 v120, v120
	v_exp_f32_e32 v122, v121
	v_exp_f32_e32 v121, v117
	v_mul_f32_e32 v116, 0x3fb8aa3b, v116
	v_mul_f32_e32 v115, 0x3fb8aa3b, v115
	v_sub_f32_e32 v37, v47, v37
	v_exp_f32_e32 v123, v116
	v_exp_f32_e32 v125, v115
	v_mul_f32_e32 v37, 0x3fb8aa3b, v37
	v_mul_f32_e32 v114, 0x3fb8aa3b, v114
	v_exp_f32_e32 v134, v37
	v_add_f32_e32 v37, v103, v35
	v_exp_f32_e32 v119, v114
	v_mul_f32_e32 v111, 0x3fb8aa3b, v111
	v_mul_f32_e32 v107, 0x3fb8aa3b, v107
	v_mul_f32_e32 v106, 0x3fb8aa3b, v106
	v_sub_f32_e32 v37, v47, v37
	v_mul_f32_e32 v113, 0x3fb8aa3b, v113
	v_exp_f32_e32 v116, v111
	v_mul_f32_e32 v109, 0x3fb8aa3b, v109
	v_mul_f32_e32 v108, 0x3fb8aa3b, v108
	v_exp_f32_e32 v117, v107
	v_exp_f32_e32 v111, v106
	v_pk_add_f32 v[106:107], v[120:121], 1.0 op_sel_hi:[1,0] neg_lo:[1,0] neg_hi:[1,0]
	v_mul_f32_e32 v37, 0x3fb8aa3b, v37
	v_exp_f32_e32 v114, v113
	v_mul_f32_e32 v112, 0x3fb8aa3b, v112
	v_exp_f32_e32 v115, v109
	v_exp_f32_e32 v113, v108
	v_pk_add_f32 v[108:109], v[122:123], 1.0 op_sel_hi:[1,0] neg_lo:[1,0] neg_hi:[1,0]
	v_pk_add_f32 v[120:121], v[124:125], 1.0 op_sel_hi:[1,0] neg_lo:[1,0] neg_hi:[1,0]
	v_and_b32_sdwa v122, v107, v75 dst_sel:DWORD dst_unused:UNUSED_PAD src0_sel:WORD_1 src1_sel:DWORD
	v_and_b32_sdwa v123, v106, v75 dst_sel:DWORD dst_unused:UNUSED_PAD src0_sel:WORD_1 src1_sel:DWORD
	v_exp_f32_e32 v133, v37
	v_add_f32_e32 v37, v102, v35
	v_exp_f32_e32 v112, v112
	v_add3_u32 v107, v107, v122, s43
	v_add3_u32 v106, v106, v123, s43
	v_and_b32_sdwa v122, v121, v75 dst_sel:DWORD dst_unused:UNUSED_PAD src0_sel:WORD_1 src1_sel:DWORD
	v_and_b32_sdwa v123, v120, v75 dst_sel:DWORD dst_unused:UNUSED_PAD src0_sel:WORD_1 src1_sel:DWORD
	v_sub_f32_e32 v37, v47, v37
	v_mul_f32_e32 v110, 0x3fb8aa3b, v110
	v_pk_add_f32 v[118:119], v[118:119], 1.0 op_sel_hi:[1,0] neg_lo:[1,0] neg_hi:[1,0]
	v_add3_u32 v122, v121, v122, s43
	v_add3_u32 v124, v120, v123, s43
	v_and_b32_e32 v121, 0xffff0000, v107
	v_and_b32_e32 v120, 0xffff0000, v106
	v_and_b32_sdwa v106, v109, v75 dst_sel:DWORD dst_unused:UNUSED_PAD src0_sel:WORD_1 src1_sel:DWORD
	v_and_b32_sdwa v107, v108, v75 dst_sel:DWORD dst_unused:UNUSED_PAD src0_sel:WORD_1 src1_sel:DWORD
	v_mul_f32_e32 v37, 0x3fb8aa3b, v37
	v_exp_f32_e32 v110, v110
	v_add3_u32 v106, v109, v106, s43
	v_add3_u32 v107, v108, v107, s43
	v_and_b32_sdwa v108, v119, v75 dst_sel:DWORD dst_unused:UNUSED_PAD src0_sel:WORD_1 src1_sel:DWORD
	v_and_b32_sdwa v109, v118, v75 dst_sel:DWORD dst_unused:UNUSED_PAD src0_sel:WORD_1 src1_sel:DWORD
	v_exp_f32_e32 v135, v37
	v_add_f32_e32 v37, v101, v35
	v_add_f32_e32 v35, v99, v35
	v_add3_u32 v108, v119, v108, s43
	v_add3_u32 v109, v118, v109, s43
	v_and_b32_e32 v119, 0xffff0000, v106
	v_and_b32_e32 v118, 0xffff0000, v107
	v_pk_add_f32 v[106:107], v[114:115], 1.0 op_sel_hi:[1,0] neg_lo:[1,0] neg_hi:[1,0]
	v_sub_f32_e32 v35, v47, v35
	v_and_b32_e32 v123, 0xffff0000, v122
	v_and_b32_e32 v122, 0xffff0000, v124
	v_and_b32_e32 v125, 0xffff0000, v108
	v_and_b32_e32 v124, 0xffff0000, v109
	v_pk_add_f32 v[108:109], v[112:113], 1.0 op_sel_hi:[1,0] neg_lo:[1,0] neg_hi:[1,0]
	v_pk_add_f32 v[112:113], v[116:117], 1.0 op_sel_hi:[1,0] neg_lo:[1,0] neg_hi:[1,0]
	v_and_b32_sdwa v114, v107, v75 dst_sel:DWORD dst_unused:UNUSED_PAD src0_sel:WORD_1 src1_sel:DWORD
	v_and_b32_sdwa v115, v106, v75 dst_sel:DWORD dst_unused:UNUSED_PAD src0_sel:WORD_1 src1_sel:DWORD
	v_sub_f32_e32 v37, v47, v37
	v_mul_f32_e32 v35, 0x3fb8aa3b, v35
	v_add3_u32 v107, v107, v114, s43
	v_add3_u32 v106, v106, v115, s43
	v_and_b32_sdwa v114, v113, v75 dst_sel:DWORD dst_unused:UNUSED_PAD src0_sel:WORD_1 src1_sel:DWORD
	v_and_b32_sdwa v115, v112, v75 dst_sel:DWORD dst_unused:UNUSED_PAD src0_sel:WORD_1 src1_sel:DWORD
	v_mul_f32_e32 v37, 0x3fb8aa3b, v37
	v_exp_f32_e32 v104, v35
	v_pk_add_f32 v[110:111], v[110:111], 1.0 op_sel_hi:[1,0] neg_lo:[1,0] neg_hi:[1,0]
	v_add3_u32 v113, v113, v114, s43
	v_add3_u32 v112, v112, v115, s43
	v_and_b32_e32 v115, 0xffff0000, v107
	v_and_b32_e32 v114, 0xffff0000, v106
	v_and_b32_sdwa v106, v109, v75 dst_sel:DWORD dst_unused:UNUSED_PAD src0_sel:WORD_1 src1_sel:DWORD
	v_and_b32_sdwa v107, v108, v75 dst_sel:DWORD dst_unused:UNUSED_PAD src0_sel:WORD_1 src1_sel:DWORD
	v_exp_f32_e32 v130, v37
	v_add3_u32 v106, v109, v106, s43
	v_add3_u32 v107, v108, v107, s43
	v_and_b32_sdwa v108, v111, v75 dst_sel:DWORD dst_unused:UNUSED_PAD src0_sel:WORD_1 src1_sel:DWORD
	v_and_b32_sdwa v109, v110, v75 dst_sel:DWORD dst_unused:UNUSED_PAD src0_sel:WORD_1 src1_sel:DWORD
	v_add3_u32 v108, v111, v108, s43
	v_add3_u32 v109, v110, v109, s43
	v_and_b32_e32 v127, 0xffff0000, v106
	v_and_b32_e32 v126, 0xffff0000, v107
	v_and_b32_e32 v129, 0xffff0000, v108
	v_and_b32_e32 v128, 0xffff0000, v109
	v_pk_mul_f32 v[104:105], v[104:105], v[126:127]
	v_pk_mul_f32 v[102:103], v[134:135], v[118:119]
	v_pk_mul_f32 v[118:119], v[130:131], v[128:129]
	v_bfe_u32 v61, v105, 16, 1
	v_bfe_u32 v35, v119, 16, 1
	v_bfe_u32 v49, v104, 16, 1
	v_add3_u32 v61, v105, v61, s43
	v_bfe_u32 v37, v118, 16, 1
	v_add3_u32 v35, v119, v35, s43
	v_bfe_u32 v45, v103, 16, 1
	v_add3_u32 v49, v104, v49, s43
	v_lshrrev_b32_e32 v61, 16, v61
	v_add3_u32 v37, v118, v37, s43
	v_bfe_u32 v43, v102, 16, 1
	v_add3_u32 v45, v103, v45, s43
	v_lshrrev_b32_e32 v49, 16, v49
	v_and_or_b32 v103, v35, s52, v61
	v_cndmask_b32_e64 v35, 0, v62, s[22:23]
	v_add3_u32 v43, v102, v43, s43
	v_and_or_b32 v102, v37, s52, v49
	v_add_f32_e32 v37, v48, v35
	v_cndmask_b32_e64 v35, v35, v37, s[20:21]
	v_add_f32_e32 v37, v42, v35
	v_cndmask_b32_e64 v35, v35, v37, s[18:19]
	v_add_f32_e32 v37, v44, v35
	v_cndmask_b32_e64 v35, v35, v37, s[16:17]
	v_add_f32_e32 v37, v38, v35
	v_cndmask_b32_e64 v35, v35, v37, s[14:15]
	v_add_f32_e32 v37, v40, v35
	v_cndmask_b32_e64 v35, v35, v37, s[12:13]
	v_add_f32_e32 v34, v34, v35
	v_cndmask_b32_e64 v34, v35, v34, s[10:11]
	v_add_f32_e32 v35, v36, v34
	v_cndmask_b32_e64 v36, v34, v35, s[8:9]
	v_add_f32_e32 v34, v60, v36
	v_sub_f32_e32 v34, v46, v34
	v_mul_f32_e32 v34, 0x3fb8aa3b, v34
	v_exp_f32_e32 v35, v34
	v_add_f32_e32 v34, v98, v36
	v_sub_f32_e32 v34, v46, v34
	v_mul_f32_e32 v34, 0x3fb8aa3b, v34
	v_exp_f32_e32 v37, v34
	v_add_f32_e32 v34, v97, v36
	v_sub_f32_e32 v34, v46, v34
	v_mul_f32_e32 v34, 0x3fb8aa3b, v34
	v_exp_f32_e32 v38, v34
	v_add_f32_e32 v34, v36, v93
	v_sub_f32_e32 v34, v46, v34
	v_mul_f32_e32 v34, 0x3fb8aa3b, v34
	v_pk_mul_f32 v[100:101], v[132:133], v[124:125]
	v_exp_f32_e32 v40, v34
	v_add_f32_e32 v34, v96, v36
	v_bfe_u32 v39, v101, 16, 1
	v_sub_f32_e32 v34, v46, v34
	v_add3_u32 v39, v101, v39, s43
	v_lshrrev_b32_e32 v45, 16, v45
	v_mul_f32_e32 v34, 0x3fb8aa3b, v34
	v_and_or_b32 v101, v39, s52, v45
	v_exp_f32_e32 v39, v34
	v_add_f32_e32 v34, v95, v36
	v_bfe_u32 v41, v100, 16, 1
	v_sub_f32_e32 v34, v46, v34
	v_add3_u32 v41, v100, v41, s43
	v_lshrrev_b32_e32 v43, 16, v43
	v_mul_f32_e32 v34, 0x3fb8aa3b, v34
	v_and_or_b32 v100, v41, s52, v43
	v_exp_f32_e32 v41, v34
	v_add_f32_e32 v34, v94, v36
	v_sub_f32_e32 v34, v46, v34
	v_add_f32_e32 v36, v92, v36
	v_mul_f32_e32 v34, 0x3fb8aa3b, v34
	v_sub_f32_e32 v36, v46, v36
	v_exp_f32_e32 v34, v34
	v_mul_f32_e32 v36, 0x3fb8aa3b, v36
	v_exp_f32_e32 v36, v36
	v_and_b32_e32 v117, 0xffff0000, v113
	v_and_b32_e32 v116, 0xffff0000, v112
	v_pk_mul_f32 v[38:39], v[38:39], v[122:123]
	v_pk_mul_f32 v[34:35], v[34:35], v[116:117]
	v_pk_mul_f32 v[40:41], v[40:41], v[120:121]
	v_pk_mul_f32 v[36:37], v[36:37], v[114:115]
	v_bfe_u32 v42, v35, 16, 1
	v_bfe_u32 v43, v34, 16, 1
	v_bfe_u32 v44, v39, 16, 1
	v_bfe_u32 v45, v38, 16, 1
	v_add3_u32 v38, v38, v45, s43
	v_add3_u32 v39, v39, v44, s43
	v_add3_u32 v34, v34, v43, s43
	v_add3_u32 v35, v35, v42, s43
	v_bfe_u32 v42, v40, 16, 1
	v_bfe_u32 v43, v41, 16, 1
	v_bfe_u32 v44, v36, 16, 1
	v_bfe_u32 v45, v37, 16, 1
	s_waitcnt vmcnt(26)
	v_lshrrev_b32_e32 v106, 16, v90
	v_add3_u32 v37, v37, v45, s43
	v_add3_u32 v36, v36, v44, s43
	v_add3_u32 v41, v41, v43, s43
	v_add3_u32 v40, v40, v42, s43
	s_waitcnt vmcnt(25)
	v_and_or_b32 v109, v91, s52, v106
	v_lshrrev_b32_e32 v106, 16, v84
	v_lshrrev_b32_e32 v107, 16, v86
	v_lshrrev_b32_e32 v108, 16, v88
	v_lshlrev_b32_e32 v110, 16, v91
	v_lshrrev_b32_e32 v40, 16, v40
	v_lshrrev_b32_e32 v41, 16, v41
	v_lshrrev_b32_e32 v36, 16, v36
	v_lshrrev_b32_e32 v37, 16, v37
	s_add_i32 s36, s39, 1
	v_and_or_b32 v106, v85, s52, v106
	v_and_or_b32 v107, v87, s52, v107
	v_and_or_b32 v108, v89, s52, v108
	v_and_or_b32 v113, v90, s53, v110
	v_lshlrev_b32_e32 v110, 16, v85
	v_lshlrev_b32_e32 v111, 16, v87
	v_lshlrev_b32_e32 v112, 16, v89
	v_and_or_b32 v37, v35, s52, v37
	v_and_or_b32 v36, v34, s52, v36
	v_and_or_b32 v35, v39, s52, v41
	v_and_or_b32 v34, v38, s52, v40
	s_cmp_ge_u32 s36, s38
	v_and_or_b32 v110, v84, s53, v110
	v_and_or_b32 v111, v86, s53, v111
	v_and_or_b32 v112, v88, s53, v112
	ds_write_b128 v70, v[34:37] offset:34816
	ds_write_b128 v70, v[100:103] offset:34960
	ds_write_b128 v70, v[110:113] offset:53248
	ds_write_b128 v70, v[106:109] offset:53392
	s_cbranch_scc1 .LBB0_1379
	s_add_i32 s40, s35, s39
	s_ashr_i32 s41, s40, 31
	s_lshl_b64 s[40:41], s[40:41], 13
	v_lshl_add_u64 v[34:35], s[40:41], 0, v[58:59]
	v_lshlrev_b64 v[34:35], 1, v[34:35]
	v_lshl_add_u64 v[36:37], s[30:31], 0, v[34:35]
	v_lshl_add_u64 v[34:35], s[28:29], 0, v[34:35]
	global_load_dword v76, v[36:37], off
	global_load_dword v77, v[36:37], off offset:256
	global_load_dword v78, v[36:37], off offset:512
	global_load_dword v79, v[36:37], off offset:768
	global_load_dword v80, v[36:37], off offset:1024
	global_load_dword v81, v[36:37], off offset:1280
	global_load_dword v82, v[36:37], off offset:1536
	global_load_dword v83, v[36:37], off offset:1792
	global_load_dword v84, v[34:35], off
	global_load_dword v85, v[34:35], off offset:256
	global_load_dword v86, v[34:35], off offset:512
	global_load_dword v87, v[34:35], off offset:768
	global_load_dword v88, v[34:35], off offset:1024
	global_load_dword v89, v[34:35], off offset:1280
	global_load_dword v90, v[34:35], off offset:1536
	global_load_dword v91, v[34:35], off offset:1792
	s_branch .LBB0_1379

.LBB0_1389:
	s_barrier
	s_and_saveexec_b64 s[10:11], s[6:7]
	s_cbranch_execz .Luv4_slot_written
	v_mov_b32_e32 v2, 0
	v_add_u32_e32 v3, 0x690, v250
	ds_write_b32 v2, v3
